# GEMM compute-segment heads (16 phases in the 4 K-loops): s_setprio 1 moved in front of the opening barrier and the redundant post-barrier lgkmcnt(0) dropped, so the first MFMA issues right at barrier
# speedup vs baseline: 1.0028x; 1.0028x over previous
.LBB0_191:
	s_add_u32 s42, s40, 0xfff80080
	s_addc_u32 s43, s41, -1
	s_add_i32 s91, 0, 0x10000
	s_cmp_eq_u32 s90, 28
	s_cselect_b32 s45, s9, s43
	s_cselect_b32 s44, s86, s42
	s_cselect_b32 s43, s11, s89
	s_cselect_b32 s42, s87, s88
	s_add_i32 s94, 0, 0x14000
	v_add_u32_e32 v160, s91, v154
	v_add_u32_e32 v176, s94, v154
	ds_read_b128 v[146:149], v160
	ds_read_b128 v[150:153], v160 offset:1024
	ds_read_b128 v[156:159], v160 offset:2048
	ds_read_b128 v[160:163], v160 offset:3072
	ds_read_b128 v[164:167], v176
	ds_read_b128 v[168:171], v176 offset:1024
	ds_read_b128 v[172:175], v176 offset:2048
	ds_read_b128 v[176:179], v176 offset:3072
	v_lshl_add_u64 v[222:223], s[40:41], 0, v[142:143]
	s_add_i32 m0, s60, 0xc000
	ds_read_b128 v[180:183], v155
	ds_read_b128 v[184:187], v155 offset:1024
	ds_read_b128 v[188:191], v155 offset:2048
	ds_read_b128 v[192:195], v155 offset:3072
	ds_read_b128 v[196:199], v155 offset:4096
	ds_read_b128 v[200:203], v155 offset:5120
	ds_read_b128 v[204:207], v155 offset:6144
	ds_read_b128 v[218:221], v155 offset:7168
	global_load_lds_dwordx4 v[222:223], off
	v_lshl_add_u64 v[222:223], s[40:41], 0, v[144:145]
	s_add_i32 m0, s60, 0xe000
	s_nop 0
	global_load_lds_dwordx4 v[222:223], off
	s_waitcnt vmcnt(8)
	s_waitcnt lgkmcnt(0)
	s_setprio 1
	s_barrier
	v_mfma_f32_16x16x32_bf16 v[128:131], v[146:149], v[180:183], v[128:131]
	v_mfma_f32_16x16x32_bf16 v[124:127], v[156:159], v[180:183], v[124:127]
	v_mfma_f32_16x16x32_bf16 v[120:123], v[146:149], v[188:191], v[120:123]
	v_mfma_f32_16x16x32_bf16 v[116:119], v[156:159], v[188:191], v[116:119]
	v_mfma_f32_16x16x32_bf16 v[112:115], v[146:149], v[196:199], v[112:115]
	v_mfma_f32_16x16x32_bf16 v[104:107], v[156:159], v[196:199], v[104:107]
	v_mfma_f32_16x16x32_bf16 v[96:99], v[146:149], v[204:207], v[96:99]
	v_mfma_f32_16x16x32_bf16 v[88:91], v[156:159], v[204:207], v[88:91]
	v_mfma_f32_16x16x32_bf16 v[128:131], v[150:153], v[184:187], v[128:131]
	v_mfma_f32_16x16x32_bf16 v[124:127], v[160:163], v[184:187], v[124:127]
	v_mfma_f32_16x16x32_bf16 v[120:123], v[150:153], v[192:195], v[120:123]
	v_mfma_f32_16x16x32_bf16 v[116:119], v[160:163], v[192:195], v[116:119]
	v_mfma_f32_16x16x32_bf16 v[112:115], v[150:153], v[200:203], v[112:115]
	v_mfma_f32_16x16x32_bf16 v[104:107], v[160:163], v[200:203], v[104:107]
	v_mfma_f32_16x16x32_bf16 v[96:99], v[150:153], v[218:221], v[96:99]
	v_mfma_f32_16x16x32_bf16 v[88:91], v[160:163], v[218:221], v[88:91]
	s_setprio 0
	s_setprio 1
	v_mfma_f32_16x16x32_bf16 v[108:111], v[164:167], v[180:183], v[108:111]
	v_mfma_f32_16x16x32_bf16 v[100:103], v[172:175], v[180:183], v[100:103]
	v_mfma_f32_16x16x32_bf16 v[92:95], v[164:167], v[188:191], v[92:95]
	v_mfma_f32_16x16x32_bf16 v[84:87], v[172:175], v[188:191], v[84:87]
	v_mfma_f32_16x16x32_bf16 v[80:83], v[164:167], v[196:199], v[80:83]
	v_mfma_f32_16x16x32_bf16 v[76:79], v[172:175], v[196:199], v[76:79]
	v_mfma_f32_16x16x32_bf16 v[72:75], v[164:167], v[204:207], v[72:75]
	v_mfma_f32_16x16x32_bf16 v[68:71], v[172:175], v[204:207], v[68:71]
	v_mfma_f32_16x16x32_bf16 v[108:111], v[168:171], v[184:187], v[108:111]
	v_mfma_f32_16x16x32_bf16 v[100:103], v[176:179], v[184:187], v[100:103]
	v_mfma_f32_16x16x32_bf16 v[92:95], v[168:171], v[192:195], v[92:95]
	v_mfma_f32_16x16x32_bf16 v[84:87], v[176:179], v[192:195], v[84:87]
	v_mfma_f32_16x16x32_bf16 v[80:83], v[168:171], v[200:203], v[80:83]
	v_mfma_f32_16x16x32_bf16 v[76:79], v[176:179], v[200:203], v[76:79]
	v_mfma_f32_16x16x32_bf16 v[72:75], v[168:171], v[218:221], v[72:75]
	v_mfma_f32_16x16x32_bf16 v[68:71], v[176:179], v[218:221], v[68:71]
	s_setprio 0
	s_barrier
	s_add_i32 s91, s91, s51
	v_lshl_add_u64 v[222:223], s[42:43], 0, v[2:3]
	s_mov_b32 m0, s91
	ds_read_b128 v[180:183], v155 offset:16384
	ds_read_b128 v[184:187], v155 offset:17408
	ds_read_b128 v[188:191], v155 offset:18432
	ds_read_b128 v[192:195], v155 offset:19456
	ds_read_b128 v[196:199], v155 offset:20480
	ds_read_b128 v[200:203], v155 offset:21504
	ds_read_b128 v[204:207], v155 offset:22528
	ds_read_b128 v[218:221], v155 offset:23552
	global_load_lds_dwordx4 v[222:223], off
	s_add_i32 m0, s91, 0x2000
	s_add_u32 s92, s42, 0x80000
	v_lshl_add_u64 v[224:225], s[42:43], 0, v[132:133]
	s_addc_u32 s93, s43, 0
	s_add_i32 s91, s94, s51
	global_load_lds_dwordx4 v[224:225], off
	v_lshl_add_u64 v[226:227], s[92:93], 0, v[2:3]
	s_mov_b32 m0, s91
	v_lshl_add_u64 v[228:229], s[44:45], 0, v[134:135]
	global_load_lds_dwordx4 v[226:227], off
	v_lshl_add_u64 v[226:227], s[92:93], 0, v[132:133]
	s_add_i32 m0, s91, 0x2000
	s_nop 0
	global_load_lds_dwordx4 v[226:227], off
	v_lshl_add_u64 v[226:227], s[44:45], 0, v[136:137]
	s_mov_b32 m0, s60
	s_nop 0
	global_load_lds_dwordx4 v[226:227], off
	s_mov_b32 m0, s61
	s_nop 0
	global_load_lds_dwordx4 v[228:229], off
	s_waitcnt vmcnt(8)
	s_waitcnt lgkmcnt(0)
	s_setprio 1
	s_barrier
	v_mfma_f32_16x16x32_bf16 v[64:67], v[146:149], v[180:183], v[64:67]
	v_mfma_f32_16x16x32_bf16 v[60:63], v[156:159], v[180:183], v[60:63]
	v_mfma_f32_16x16x32_bf16 v[56:59], v[146:149], v[188:191], v[56:59]
	v_mfma_f32_16x16x32_bf16 v[52:55], v[156:159], v[188:191], v[52:55]
	v_mfma_f32_16x16x32_bf16 v[40:43], v[146:149], v[196:199], v[40:43]
	v_mfma_f32_16x16x32_bf16 v[36:39], v[156:159], v[196:199], v[36:39]
	v_mfma_f32_16x16x32_bf16 v[24:27], v[146:149], v[204:207], v[24:27]
	v_mfma_f32_16x16x32_bf16 v[20:23], v[156:159], v[204:207], v[20:23]
	v_mfma_f32_16x16x32_bf16 v[64:67], v[150:153], v[184:187], v[64:67]
	v_mfma_f32_16x16x32_bf16 v[60:63], v[160:163], v[184:187], v[60:63]
	v_mfma_f32_16x16x32_bf16 v[56:59], v[150:153], v[192:195], v[56:59]
	v_mfma_f32_16x16x32_bf16 v[52:55], v[160:163], v[192:195], v[52:55]
	v_mfma_f32_16x16x32_bf16 v[40:43], v[150:153], v[200:203], v[40:43]
	v_mfma_f32_16x16x32_bf16 v[36:39], v[160:163], v[200:203], v[36:39]
	v_mfma_f32_16x16x32_bf16 v[24:27], v[150:153], v[218:221], v[24:27]
	v_mfma_f32_16x16x32_bf16 v[20:23], v[160:163], v[218:221], v[20:23]
	s_setprio 0
	s_setprio 1
	v_mfma_f32_16x16x32_bf16 v[48:51], v[164:167], v[180:183], v[48:51]
	v_mfma_f32_16x16x32_bf16 v[44:47], v[172:175], v[180:183], v[44:47]
	v_mfma_f32_16x16x32_bf16 v[32:35], v[164:167], v[188:191], v[32:35]
	v_mfma_f32_16x16x32_bf16 v[28:31], v[172:175], v[188:191], v[28:31]
	v_mfma_f32_16x16x32_bf16 v[16:19], v[164:167], v[196:199], v[16:19]
	v_mfma_f32_16x16x32_bf16 v[12:15], v[172:175], v[196:199], v[12:15]
	v_mfma_f32_16x16x32_bf16 v[8:11], v[164:167], v[204:207], v[8:11]
	v_mfma_f32_16x16x32_bf16 v[4:7], v[172:175], v[204:207], v[4:7]
	v_mfma_f32_16x16x32_bf16 v[48:51], v[168:171], v[184:187], v[48:51]
	v_mfma_f32_16x16x32_bf16 v[44:47], v[176:179], v[184:187], v[44:47]
	v_mfma_f32_16x16x32_bf16 v[32:35], v[168:171], v[192:195], v[32:35]
	v_mfma_f32_16x16x32_bf16 v[28:31], v[176:179], v[192:195], v[28:31]
	v_mfma_f32_16x16x32_bf16 v[16:19], v[168:171], v[200:203], v[16:19]
	v_mfma_f32_16x16x32_bf16 v[12:15], v[176:179], v[200:203], v[12:15]
	v_mfma_f32_16x16x32_bf16 v[8:11], v[168:171], v[218:221], v[8:11]
	v_mfma_f32_16x16x32_bf16 v[4:7], v[176:179], v[218:221], v[4:7]
	s_setprio 0
	s_barrier
	s_add_i32 s91, 0, 0x18000
	s_add_i32 s92, 0, 0x1c000
	v_add_u32_e32 v160, s91, v154
	v_add_u32_e32 v176, s92, v154
	ds_read_b128 v[146:149], v160
	ds_read_b128 v[150:153], v160 offset:1024
	ds_read_b128 v[156:159], v160 offset:2048
	ds_read_b128 v[160:163], v160 offset:3072
	ds_read_b128 v[164:167], v176
	ds_read_b128 v[168:171], v176 offset:1024
	ds_read_b128 v[172:175], v176 offset:2048
	ds_read_b128 v[176:179], v176 offset:3072
	s_add_u32 s44, s44, 0x80000
	s_addc_u32 s45, s45, 0
	s_mov_b32 m0, s80
	v_lshl_add_u64 v[230:231], s[44:45], 0, v[136:137]
	ds_read_b128 v[180:183], v155 offset:32768
	ds_read_b128 v[184:187], v155 offset:33792
	ds_read_b128 v[188:191], v155 offset:34816
	ds_read_b128 v[192:195], v155 offset:35840
	ds_read_b128 v[196:199], v155 offset:36864
	ds_read_b128 v[200:203], v155 offset:37888
	ds_read_b128 v[204:207], v155 offset:38912
	ds_read_b128 v[218:221], v155 offset:39936
	global_load_lds_dwordx4 v[230:231], off
	v_lshl_add_u64 v[230:231], s[44:45], 0, v[134:135]
	s_mov_b32 m0, s81
	s_nop 0
	global_load_lds_dwordx4 v[230:231], off
	s_waitcnt vmcnt(8)
	s_waitcnt lgkmcnt(0)
	s_setprio 1
	s_barrier
	v_mfma_f32_16x16x32_bf16 v[128:131], v[146:149], v[180:183], v[128:131]
	v_mfma_f32_16x16x32_bf16 v[124:127], v[156:159], v[180:183], v[124:127]
	v_mfma_f32_16x16x32_bf16 v[120:123], v[146:149], v[188:191], v[120:123]
	v_mfma_f32_16x16x32_bf16 v[116:119], v[156:159], v[188:191], v[116:119]
	v_mfma_f32_16x16x32_bf16 v[112:115], v[146:149], v[196:199], v[112:115]
	v_mfma_f32_16x16x32_bf16 v[104:107], v[156:159], v[196:199], v[104:107]
	v_mfma_f32_16x16x32_bf16 v[96:99], v[146:149], v[204:207], v[96:99]
	v_mfma_f32_16x16x32_bf16 v[88:91], v[156:159], v[204:207], v[88:91]
	v_mfma_f32_16x16x32_bf16 v[128:131], v[150:153], v[184:187], v[128:131]
	v_mfma_f32_16x16x32_bf16 v[124:127], v[160:163], v[184:187], v[124:127]
	v_mfma_f32_16x16x32_bf16 v[120:123], v[150:153], v[192:195], v[120:123]
	v_mfma_f32_16x16x32_bf16 v[116:119], v[160:163], v[192:195], v[116:119]
	v_mfma_f32_16x16x32_bf16 v[112:115], v[150:153], v[200:203], v[112:115]
	v_mfma_f32_16x16x32_bf16 v[104:107], v[160:163], v[200:203], v[104:107]
	v_mfma_f32_16x16x32_bf16 v[96:99], v[150:153], v[218:221], v[96:99]
	v_mfma_f32_16x16x32_bf16 v[88:91], v[160:163], v[218:221], v[88:91]
	s_setprio 0
	s_setprio 1
	v_mfma_f32_16x16x32_bf16 v[108:111], v[164:167], v[180:183], v[108:111]
	v_mfma_f32_16x16x32_bf16 v[100:103], v[172:175], v[180:183], v[100:103]
	v_mfma_f32_16x16x32_bf16 v[92:95], v[164:167], v[188:191], v[92:95]
	v_mfma_f32_16x16x32_bf16 v[84:87], v[172:175], v[188:191], v[84:87]
	v_mfma_f32_16x16x32_bf16 v[80:83], v[164:167], v[196:199], v[80:83]
	v_mfma_f32_16x16x32_bf16 v[76:79], v[172:175], v[196:199], v[76:79]
	v_mfma_f32_16x16x32_bf16 v[72:75], v[164:167], v[204:207], v[72:75]
	v_mfma_f32_16x16x32_bf16 v[68:71], v[172:175], v[204:207], v[68:71]
	v_mfma_f32_16x16x32_bf16 v[108:111], v[168:171], v[184:187], v[108:111]
	v_mfma_f32_16x16x32_bf16 v[100:103], v[176:179], v[184:187], v[100:103]
	v_mfma_f32_16x16x32_bf16 v[92:95], v[168:171], v[192:195], v[92:95]
	v_mfma_f32_16x16x32_bf16 v[84:87], v[176:179], v[192:195], v[84:87]
	v_mfma_f32_16x16x32_bf16 v[80:83], v[168:171], v[200:203], v[80:83]
	v_mfma_f32_16x16x32_bf16 v[76:79], v[176:179], v[200:203], v[76:79]
	v_mfma_f32_16x16x32_bf16 v[72:75], v[168:171], v[218:221], v[72:75]
	v_mfma_f32_16x16x32_bf16 v[68:71], v[176:179], v[218:221], v[68:71]
	s_setprio 0
	s_barrier
	s_add_i32 s44, s91, s51
	v_lshl_add_u64 v[222:223], v[222:223], 0, s[16:17]
	s_mov_b32 m0, s44
	ds_read_b128 v[180:183], v155 offset:49152
	ds_read_b128 v[184:187], v155 offset:50176
	ds_read_b128 v[188:191], v155 offset:51200
	ds_read_b128 v[192:195], v155 offset:52224
	ds_read_b128 v[196:199], v155 offset:53248
	ds_read_b128 v[200:203], v155 offset:54272
	ds_read_b128 v[204:207], v155 offset:55296
	ds_read_b128 v[218:221], v155 offset:56320
	global_load_lds_dwordx4 v[222:223], off
	s_add_i32 m0, s44, 0x2000
	s_add_u32 s42, s42, 0x80080
	v_lshl_add_u64 v[222:223], v[224:225], 0, s[16:17]
	s_addc_u32 s43, s43, 0
	s_add_i32 s44, s92, s51
	global_load_lds_dwordx4 v[222:223], off
	v_lshl_add_u64 v[222:223], s[42:43], 0, v[2:3]
	s_mov_b32 m0, s44
	s_nop 0
	global_load_lds_dwordx4 v[222:223], off
	v_lshl_add_u64 v[222:223], s[42:43], 0, v[132:133]
	s_add_i32 m0, s44, 0x2000
	s_nop 0
	global_load_lds_dwordx4 v[222:223], off
	v_lshl_add_u64 v[222:223], v[226:227], 0, s[16:17]
	s_mov_b32 m0, s82
	s_nop 0
	global_load_lds_dwordx4 v[222:223], off
	v_lshl_add_u64 v[222:223], v[228:229], 0, s[16:17]
	s_mov_b32 m0, s83
	s_nop 0
	global_load_lds_dwordx4 v[222:223], off
	s_waitcnt vmcnt(8)
	s_waitcnt lgkmcnt(0)
	s_setprio 1
	s_barrier
	v_mfma_f32_16x16x32_bf16 v[64:67], v[146:149], v[180:183], v[64:67]
	v_mfma_f32_16x16x32_bf16 v[60:63], v[156:159], v[180:183], v[60:63]
	v_mfma_f32_16x16x32_bf16 v[56:59], v[146:149], v[188:191], v[56:59]
	v_mfma_f32_16x16x32_bf16 v[52:55], v[156:159], v[188:191], v[52:55]
	v_mfma_f32_16x16x32_bf16 v[40:43], v[146:149], v[196:199], v[40:43]
	v_mfma_f32_16x16x32_bf16 v[36:39], v[156:159], v[196:199], v[36:39]
	v_mfma_f32_16x16x32_bf16 v[24:27], v[146:149], v[204:207], v[24:27]
	v_mfma_f32_16x16x32_bf16 v[20:23], v[156:159], v[204:207], v[20:23]
	v_mfma_f32_16x16x32_bf16 v[64:67], v[150:153], v[184:187], v[64:67]
	v_mfma_f32_16x16x32_bf16 v[60:63], v[160:163], v[184:187], v[60:63]
	v_mfma_f32_16x16x32_bf16 v[56:59], v[150:153], v[192:195], v[56:59]
	v_mfma_f32_16x16x32_bf16 v[52:55], v[160:163], v[192:195], v[52:55]
	v_mfma_f32_16x16x32_bf16 v[40:43], v[150:153], v[200:203], v[40:43]
	v_mfma_f32_16x16x32_bf16 v[36:39], v[160:163], v[200:203], v[36:39]
	v_mfma_f32_16x16x32_bf16 v[24:27], v[150:153], v[218:221], v[24:27]
	v_mfma_f32_16x16x32_bf16 v[20:23], v[160:163], v[218:221], v[20:23]
	s_setprio 0
	s_setprio 1
	v_mfma_f32_16x16x32_bf16 v[48:51], v[164:167], v[180:183], v[48:51]
	v_mfma_f32_16x16x32_bf16 v[44:47], v[172:175], v[180:183], v[44:47]
	v_mfma_f32_16x16x32_bf16 v[32:35], v[164:167], v[188:191], v[32:35]
	v_mfma_f32_16x16x32_bf16 v[28:31], v[172:175], v[188:191], v[28:31]
	v_mfma_f32_16x16x32_bf16 v[16:19], v[164:167], v[196:199], v[16:19]
	v_mfma_f32_16x16x32_bf16 v[12:15], v[172:175], v[196:199], v[12:15]
	v_mfma_f32_16x16x32_bf16 v[8:11], v[164:167], v[204:207], v[8:11]
	v_mfma_f32_16x16x32_bf16 v[4:7], v[172:175], v[204:207], v[4:7]
	v_mfma_f32_16x16x32_bf16 v[48:51], v[168:171], v[184:187], v[48:51]
	v_mfma_f32_16x16x32_bf16 v[44:47], v[176:179], v[184:187], v[44:47]
	v_mfma_f32_16x16x32_bf16 v[32:35], v[168:171], v[192:195], v[32:35]
	v_mfma_f32_16x16x32_bf16 v[28:31], v[176:179], v[192:195], v[28:31]
	v_mfma_f32_16x16x32_bf16 v[16:19], v[168:171], v[200:203], v[16:19]
	v_mfma_f32_16x16x32_bf16 v[12:15], v[176:179], v[200:203], v[12:15]
	v_mfma_f32_16x16x32_bf16 v[8:11], v[168:171], v[218:221], v[8:11]
	v_mfma_f32_16x16x32_bf16 v[4:7], v[176:179], v[218:221], v[4:7]
	s_setprio 0
	s_barrier
	s_add_i32 s90, s90, 2
	s_add_u32 s40, s40, 0x100
	s_addc_u32 s41, s41, 0
	s_add_u32 s88, s88, 0x100
	s_addc_u32 s89, s89, 0
	s_cmp_gt_u32 s90, 29
	s_cbranch_scc0 .LBB0_191
	s_and_b64 vcc, exec, s[6:7]
	s_cbranch_vccz .LBB0_194
	s_barrier

.LBB0_661:
	s_add_u32 s42, s40, 0xfffc0080
	s_addc_u32 s43, s41, -1
	s_add_i32 s89, 0, 0x10000
	s_cmp_eq_u32 s88, 12
	s_cselect_b32 s45, s37, s43
	s_cselect_b32 s44, s36, s42
	s_cselect_b32 s43, s11, s87
	s_cselect_b32 s42, s13, s86
	s_add_i32 s92, 0, 0x14000
	v_add_u32_e32 v158, s89, v144
	v_add_u32_e32 v174, s92, v144
	ds_read_b128 v[146:149], v158
	ds_read_b128 v[150:153], v158 offset:1024
	ds_read_b128 v[154:157], v158 offset:2048
	ds_read_b128 v[158:161], v158 offset:3072
	ds_read_b128 v[162:165], v174
	ds_read_b128 v[166:169], v174 offset:1024
	ds_read_b128 v[170:173], v174 offset:2048
	ds_read_b128 v[174:177], v174 offset:3072
	v_lshl_add_u64 v[206:207], s[40:41], 0, v[140:141]
	s_add_i32 m0, s51, 0xc000
	ds_read_b128 v[178:181], v145
	ds_read_b128 v[182:185], v145 offset:1024
	ds_read_b128 v[186:189], v145 offset:2048
	ds_read_b128 v[190:193], v145 offset:3072
	ds_read_b128 v[194:197], v145 offset:4096
	ds_read_b128 v[198:201], v145 offset:5120
	ds_read_b128 v[202:205], v145 offset:6144
	ds_read_b128 v[218:221], v145 offset:7168
	global_load_lds_dwordx4 v[206:207], off
	v_lshl_add_u64 v[206:207], s[40:41], 0, v[142:143]
	s_add_i32 m0, s51, 0xe000
	s_nop 0
	global_load_lds_dwordx4 v[206:207], off
	s_waitcnt vmcnt(8)
	s_waitcnt lgkmcnt(0)
	s_setprio 1
	s_barrier
	v_mfma_f32_16x16x32_bf16 v[128:131], v[146:149], v[178:181], v[128:131]
	v_mfma_f32_16x16x32_bf16 v[124:127], v[154:157], v[178:181], v[124:127]
	v_mfma_f32_16x16x32_bf16 v[120:123], v[146:149], v[186:189], v[120:123]
	v_mfma_f32_16x16x32_bf16 v[116:119], v[154:157], v[186:189], v[116:119]
	v_mfma_f32_16x16x32_bf16 v[104:107], v[146:149], v[194:197], v[104:107]
	v_mfma_f32_16x16x32_bf16 v[100:103], v[154:157], v[194:197], v[100:103]
	v_mfma_f32_16x16x32_bf16 v[88:91], v[146:149], v[202:205], v[88:91]
	v_mfma_f32_16x16x32_bf16 v[84:87], v[154:157], v[202:205], v[84:87]
	v_mfma_f32_16x16x32_bf16 v[128:131], v[150:153], v[182:185], v[128:131]
	v_mfma_f32_16x16x32_bf16 v[124:127], v[158:161], v[182:185], v[124:127]
	v_mfma_f32_16x16x32_bf16 v[120:123], v[150:153], v[190:193], v[120:123]
	v_mfma_f32_16x16x32_bf16 v[116:119], v[158:161], v[190:193], v[116:119]
	v_mfma_f32_16x16x32_bf16 v[104:107], v[150:153], v[198:201], v[104:107]
	v_mfma_f32_16x16x32_bf16 v[100:103], v[158:161], v[198:201], v[100:103]
	v_mfma_f32_16x16x32_bf16 v[88:91], v[150:153], v[218:221], v[88:91]
	v_mfma_f32_16x16x32_bf16 v[84:87], v[158:161], v[218:221], v[84:87]
	s_setprio 0
	s_setprio 1
	v_mfma_f32_16x16x32_bf16 v[112:115], v[162:165], v[178:181], v[112:115]
	v_mfma_f32_16x16x32_bf16 v[108:111], v[170:173], v[178:181], v[108:111]
	v_mfma_f32_16x16x32_bf16 v[96:99], v[162:165], v[186:189], v[96:99]
	v_mfma_f32_16x16x32_bf16 v[92:95], v[170:173], v[186:189], v[92:95]
	v_mfma_f32_16x16x32_bf16 v[80:83], v[162:165], v[194:197], v[80:83]
	v_mfma_f32_16x16x32_bf16 v[76:79], v[170:173], v[194:197], v[76:79]
	v_mfma_f32_16x16x32_bf16 v[72:75], v[162:165], v[202:205], v[72:75]
	v_mfma_f32_16x16x32_bf16 v[68:71], v[170:173], v[202:205], v[68:71]
	v_mfma_f32_16x16x32_bf16 v[112:115], v[166:169], v[182:185], v[112:115]
	v_mfma_f32_16x16x32_bf16 v[108:111], v[174:177], v[182:185], v[108:111]
	v_mfma_f32_16x16x32_bf16 v[96:99], v[166:169], v[190:193], v[96:99]
	v_mfma_f32_16x16x32_bf16 v[92:95], v[174:177], v[190:193], v[92:95]
	v_mfma_f32_16x16x32_bf16 v[80:83], v[166:169], v[198:201], v[80:83]
	v_mfma_f32_16x16x32_bf16 v[76:79], v[174:177], v[198:201], v[76:79]
	v_mfma_f32_16x16x32_bf16 v[72:75], v[166:169], v[218:221], v[72:75]
	v_mfma_f32_16x16x32_bf16 v[68:71], v[174:177], v[218:221], v[68:71]
	s_setprio 0
	s_barrier
	s_add_i32 s89, s89, s49
	v_lshl_add_u64 v[206:207], s[42:43], 0, v[136:137]
	s_mov_b32 m0, s89
	ds_read_b128 v[178:181], v145 offset:16384
	ds_read_b128 v[182:185], v145 offset:17408
	ds_read_b128 v[186:189], v145 offset:18432
	ds_read_b128 v[190:193], v145 offset:19456
	ds_read_b128 v[194:197], v145 offset:20480
	ds_read_b128 v[198:201], v145 offset:21504
	ds_read_b128 v[202:205], v145 offset:22528
	ds_read_b128 v[218:221], v145 offset:23552
	global_load_lds_dwordx4 v[206:207], off
	s_add_i32 m0, s89, 0x2000
	s_add_u32 s90, s42, 0x40000
	v_lshl_add_u64 v[222:223], s[42:43], 0, v[132:133]
	s_addc_u32 s91, s43, 0
	s_add_i32 s89, s92, s49
	global_load_lds_dwordx4 v[222:223], off
	v_lshl_add_u64 v[224:225], s[90:91], 0, v[136:137]
	s_mov_b32 m0, s89
	v_lshl_add_u64 v[226:227], s[44:45], 0, v[134:135]
	global_load_lds_dwordx4 v[224:225], off
	v_lshl_add_u64 v[224:225], s[90:91], 0, v[132:133]
	s_add_i32 m0, s89, 0x2000
	s_nop 0
	global_load_lds_dwordx4 v[224:225], off
	v_lshl_add_u64 v[224:225], s[44:45], 0, v[138:139]
	s_mov_b32 m0, s51
	s_nop 0
	global_load_lds_dwordx4 v[224:225], off
	s_mov_b32 m0, s60
	s_nop 0
	global_load_lds_dwordx4 v[226:227], off
	s_waitcnt vmcnt(8)
	s_waitcnt lgkmcnt(0)
	s_setprio 1
	s_barrier
	v_mfma_f32_16x16x32_bf16 v[64:67], v[146:149], v[178:181], v[64:67]
	v_mfma_f32_16x16x32_bf16 v[60:63], v[154:157], v[178:181], v[60:63]
	v_mfma_f32_16x16x32_bf16 v[56:59], v[146:149], v[186:189], v[56:59]
	v_mfma_f32_16x16x32_bf16 v[52:55], v[154:157], v[186:189], v[52:55]
	v_mfma_f32_16x16x32_bf16 v[40:43], v[146:149], v[194:197], v[40:43]
	v_mfma_f32_16x16x32_bf16 v[36:39], v[154:157], v[194:197], v[36:39]
	v_mfma_f32_16x16x32_bf16 v[24:27], v[146:149], v[202:205], v[24:27]
	v_mfma_f32_16x16x32_bf16 v[20:23], v[154:157], v[202:205], v[20:23]
	v_mfma_f32_16x16x32_bf16 v[64:67], v[150:153], v[182:185], v[64:67]
	v_mfma_f32_16x16x32_bf16 v[60:63], v[158:161], v[182:185], v[60:63]
	v_mfma_f32_16x16x32_bf16 v[56:59], v[150:153], v[190:193], v[56:59]
	v_mfma_f32_16x16x32_bf16 v[52:55], v[158:161], v[190:193], v[52:55]
	v_mfma_f32_16x16x32_bf16 v[40:43], v[150:153], v[198:201], v[40:43]
	v_mfma_f32_16x16x32_bf16 v[36:39], v[158:161], v[198:201], v[36:39]
	v_mfma_f32_16x16x32_bf16 v[24:27], v[150:153], v[218:221], v[24:27]
	v_mfma_f32_16x16x32_bf16 v[20:23], v[158:161], v[218:221], v[20:23]
	s_setprio 0
	s_setprio 1
	v_mfma_f32_16x16x32_bf16 v[48:51], v[162:165], v[178:181], v[48:51]
	v_mfma_f32_16x16x32_bf16 v[44:47], v[170:173], v[178:181], v[44:47]
	v_mfma_f32_16x16x32_bf16 v[32:35], v[162:165], v[186:189], v[32:35]
	v_mfma_f32_16x16x32_bf16 v[28:31], v[170:173], v[186:189], v[28:31]
	v_mfma_f32_16x16x32_bf16 v[16:19], v[162:165], v[194:197], v[16:19]
	v_mfma_f32_16x16x32_bf16 v[12:15], v[170:173], v[194:197], v[12:15]
	v_mfma_f32_16x16x32_bf16 v[8:11], v[162:165], v[202:205], v[8:11]
	v_mfma_f32_16x16x32_bf16 v[4:7], v[170:173], v[202:205], v[4:7]
	v_mfma_f32_16x16x32_bf16 v[48:51], v[166:169], v[182:185], v[48:51]
	v_mfma_f32_16x16x32_bf16 v[44:47], v[174:177], v[182:185], v[44:47]
	v_mfma_f32_16x16x32_bf16 v[32:35], v[166:169], v[190:193], v[32:35]
	v_mfma_f32_16x16x32_bf16 v[28:31], v[174:177], v[190:193], v[28:31]
	v_mfma_f32_16x16x32_bf16 v[16:19], v[166:169], v[198:201], v[16:19]
	v_mfma_f32_16x16x32_bf16 v[12:15], v[174:177], v[198:201], v[12:15]
	v_mfma_f32_16x16x32_bf16 v[8:11], v[166:169], v[218:221], v[8:11]
	v_mfma_f32_16x16x32_bf16 v[4:7], v[174:177], v[218:221], v[4:7]
	s_setprio 0
	s_barrier
	s_add_i32 s89, 0, 0x18000
	s_add_i32 s90, 0, 0x1c000
	v_add_u32_e32 v158, s89, v144
	v_add_u32_e32 v174, s90, v144
	ds_read_b128 v[146:149], v158
	ds_read_b128 v[150:153], v158 offset:1024
	ds_read_b128 v[154:157], v158 offset:2048
	ds_read_b128 v[158:161], v158 offset:3072
	ds_read_b128 v[162:165], v174
	ds_read_b128 v[166:169], v174 offset:1024
	ds_read_b128 v[170:173], v174 offset:2048
	ds_read_b128 v[174:177], v174 offset:3072
	s_add_u32 s44, s44, 0x40000
	s_addc_u32 s45, s45, 0
	s_mov_b32 m0, s61
	v_lshl_add_u64 v[228:229], s[44:45], 0, v[138:139]
	ds_read_b128 v[178:181], v145 offset:32768
	ds_read_b128 v[182:185], v145 offset:33792
	ds_read_b128 v[186:189], v145 offset:34816
	ds_read_b128 v[190:193], v145 offset:35840
	ds_read_b128 v[194:197], v145 offset:36864
	ds_read_b128 v[198:201], v145 offset:37888
	ds_read_b128 v[202:205], v145 offset:38912
	ds_read_b128 v[218:221], v145 offset:39936
	global_load_lds_dwordx4 v[228:229], off
	v_lshl_add_u64 v[228:229], s[44:45], 0, v[134:135]
	s_mov_b32 m0, s80
	s_nop 0
	global_load_lds_dwordx4 v[228:229], off
	s_waitcnt vmcnt(8)
	s_waitcnt lgkmcnt(0)
	s_setprio 1
	s_barrier
	v_mfma_f32_16x16x32_bf16 v[128:131], v[146:149], v[178:181], v[128:131]
	v_mfma_f32_16x16x32_bf16 v[124:127], v[154:157], v[178:181], v[124:127]
	v_mfma_f32_16x16x32_bf16 v[120:123], v[146:149], v[186:189], v[120:123]
	v_mfma_f32_16x16x32_bf16 v[116:119], v[154:157], v[186:189], v[116:119]
	v_mfma_f32_16x16x32_bf16 v[104:107], v[146:149], v[194:197], v[104:107]
	v_mfma_f32_16x16x32_bf16 v[100:103], v[154:157], v[194:197], v[100:103]
	v_mfma_f32_16x16x32_bf16 v[88:91], v[146:149], v[202:205], v[88:91]
	v_mfma_f32_16x16x32_bf16 v[84:87], v[154:157], v[202:205], v[84:87]
	v_mfma_f32_16x16x32_bf16 v[128:131], v[150:153], v[182:185], v[128:131]
	v_mfma_f32_16x16x32_bf16 v[124:127], v[158:161], v[182:185], v[124:127]
	v_mfma_f32_16x16x32_bf16 v[120:123], v[150:153], v[190:193], v[120:123]
	v_mfma_f32_16x16x32_bf16 v[116:119], v[158:161], v[190:193], v[116:119]
	v_mfma_f32_16x16x32_bf16 v[104:107], v[150:153], v[198:201], v[104:107]
	v_mfma_f32_16x16x32_bf16 v[100:103], v[158:161], v[198:201], v[100:103]
	v_mfma_f32_16x16x32_bf16 v[88:91], v[150:153], v[218:221], v[88:91]
	v_mfma_f32_16x16x32_bf16 v[84:87], v[158:161], v[218:221], v[84:87]
	s_setprio 0
	s_setprio 1
	v_mfma_f32_16x16x32_bf16 v[112:115], v[162:165], v[178:181], v[112:115]
	v_mfma_f32_16x16x32_bf16 v[108:111], v[170:173], v[178:181], v[108:111]
	v_mfma_f32_16x16x32_bf16 v[96:99], v[162:165], v[186:189], v[96:99]
	v_mfma_f32_16x16x32_bf16 v[92:95], v[170:173], v[186:189], v[92:95]
	v_mfma_f32_16x16x32_bf16 v[80:83], v[162:165], v[194:197], v[80:83]
	v_mfma_f32_16x16x32_bf16 v[76:79], v[170:173], v[194:197], v[76:79]
	v_mfma_f32_16x16x32_bf16 v[72:75], v[162:165], v[202:205], v[72:75]
	v_mfma_f32_16x16x32_bf16 v[68:71], v[170:173], v[202:205], v[68:71]
	v_mfma_f32_16x16x32_bf16 v[112:115], v[166:169], v[182:185], v[112:115]
	v_mfma_f32_16x16x32_bf16 v[108:111], v[174:177], v[182:185], v[108:111]
	v_mfma_f32_16x16x32_bf16 v[96:99], v[166:169], v[190:193], v[96:99]
	v_mfma_f32_16x16x32_bf16 v[92:95], v[174:177], v[190:193], v[92:95]
	v_mfma_f32_16x16x32_bf16 v[80:83], v[166:169], v[198:201], v[80:83]
	v_mfma_f32_16x16x32_bf16 v[76:79], v[174:177], v[198:201], v[76:79]
	v_mfma_f32_16x16x32_bf16 v[72:75], v[166:169], v[218:221], v[72:75]
	v_mfma_f32_16x16x32_bf16 v[68:71], v[174:177], v[218:221], v[68:71]
	s_setprio 0
	s_barrier
	s_add_i32 s44, s89, s49
	v_lshl_add_u64 v[206:207], v[206:207], 0, s[16:17]
	s_mov_b32 m0, s44
	ds_read_b128 v[178:181], v145 offset:49152
	ds_read_b128 v[182:185], v145 offset:50176
	ds_read_b128 v[186:189], v145 offset:51200
	ds_read_b128 v[190:193], v145 offset:52224
	ds_read_b128 v[194:197], v145 offset:53248
	ds_read_b128 v[198:201], v145 offset:54272
	ds_read_b128 v[202:205], v145 offset:55296
	ds_read_b128 v[218:221], v145 offset:56320
	global_load_lds_dwordx4 v[206:207], off
	s_add_i32 m0, s44, 0x2000
	s_add_u32 s42, s42, 0x40080
	v_lshl_add_u64 v[206:207], v[222:223], 0, s[16:17]
	s_addc_u32 s43, s43, 0
	s_add_i32 s44, s90, s49
	global_load_lds_dwordx4 v[206:207], off
	v_lshl_add_u64 v[206:207], s[42:43], 0, v[136:137]
	s_mov_b32 m0, s44
	s_nop 0
	global_load_lds_dwordx4 v[206:207], off
	v_lshl_add_u64 v[206:207], s[42:43], 0, v[132:133]
	s_add_i32 m0, s44, 0x2000
	s_nop 0
	global_load_lds_dwordx4 v[206:207], off
	v_lshl_add_u64 v[206:207], v[224:225], 0, s[16:17]
	s_mov_b32 m0, s81
	s_nop 0
	global_load_lds_dwordx4 v[206:207], off
	v_lshl_add_u64 v[206:207], v[226:227], 0, s[16:17]
	s_mov_b32 m0, s82
	s_nop 0
	global_load_lds_dwordx4 v[206:207], off
	s_waitcnt vmcnt(8)
	s_waitcnt lgkmcnt(0)
	s_setprio 1
	s_barrier
	v_mfma_f32_16x16x32_bf16 v[64:67], v[146:149], v[178:181], v[64:67]
	v_mfma_f32_16x16x32_bf16 v[60:63], v[154:157], v[178:181], v[60:63]
	v_mfma_f32_16x16x32_bf16 v[56:59], v[146:149], v[186:189], v[56:59]
	v_mfma_f32_16x16x32_bf16 v[52:55], v[154:157], v[186:189], v[52:55]
	v_mfma_f32_16x16x32_bf16 v[40:43], v[146:149], v[194:197], v[40:43]
	v_mfma_f32_16x16x32_bf16 v[36:39], v[154:157], v[194:197], v[36:39]
	v_mfma_f32_16x16x32_bf16 v[24:27], v[146:149], v[202:205], v[24:27]
	v_mfma_f32_16x16x32_bf16 v[20:23], v[154:157], v[202:205], v[20:23]
	v_mfma_f32_16x16x32_bf16 v[64:67], v[150:153], v[182:185], v[64:67]
	v_mfma_f32_16x16x32_bf16 v[60:63], v[158:161], v[182:185], v[60:63]
	v_mfma_f32_16x16x32_bf16 v[56:59], v[150:153], v[190:193], v[56:59]
	v_mfma_f32_16x16x32_bf16 v[52:55], v[158:161], v[190:193], v[52:55]
	v_mfma_f32_16x16x32_bf16 v[40:43], v[150:153], v[198:201], v[40:43]
	v_mfma_f32_16x16x32_bf16 v[36:39], v[158:161], v[198:201], v[36:39]
	v_mfma_f32_16x16x32_bf16 v[24:27], v[150:153], v[218:221], v[24:27]
	v_mfma_f32_16x16x32_bf16 v[20:23], v[158:161], v[218:221], v[20:23]
	s_setprio 0
	s_setprio 1
	v_mfma_f32_16x16x32_bf16 v[48:51], v[162:165], v[178:181], v[48:51]
	v_mfma_f32_16x16x32_bf16 v[44:47], v[170:173], v[178:181], v[44:47]
	v_mfma_f32_16x16x32_bf16 v[32:35], v[162:165], v[186:189], v[32:35]
	v_mfma_f32_16x16x32_bf16 v[28:31], v[170:173], v[186:189], v[28:31]
	v_mfma_f32_16x16x32_bf16 v[16:19], v[162:165], v[194:197], v[16:19]
	v_mfma_f32_16x16x32_bf16 v[12:15], v[170:173], v[194:197], v[12:15]
	v_mfma_f32_16x16x32_bf16 v[8:11], v[162:165], v[202:205], v[8:11]
	v_mfma_f32_16x16x32_bf16 v[4:7], v[170:173], v[202:205], v[4:7]
	v_mfma_f32_16x16x32_bf16 v[48:51], v[166:169], v[182:185], v[48:51]
	v_mfma_f32_16x16x32_bf16 v[44:47], v[174:177], v[182:185], v[44:47]
	v_mfma_f32_16x16x32_bf16 v[32:35], v[166:169], v[190:193], v[32:35]
	v_mfma_f32_16x16x32_bf16 v[28:31], v[174:177], v[190:193], v[28:31]
	v_mfma_f32_16x16x32_bf16 v[16:19], v[166:169], v[198:201], v[16:19]
	v_mfma_f32_16x16x32_bf16 v[12:15], v[174:177], v[198:201], v[12:15]
	v_mfma_f32_16x16x32_bf16 v[8:11], v[166:169], v[218:221], v[8:11]
	v_mfma_f32_16x16x32_bf16 v[4:7], v[174:177], v[218:221], v[4:7]
	s_setprio 0
	s_barrier
	s_add_i32 s88, s88, 2
	s_add_u32 s40, s40, 0x100
	s_addc_u32 s41, s41, 0
	s_add_u32 s86, s86, 0x100
	s_addc_u32 s87, s87, 0
	s_cmp_gt_u32 s88, 13
	s_cbranch_scc0 .LBB0_661
	s_and_b64 vcc, exec, s[8:9]
	s_cbranch_vccz .LBB0_664
	s_barrier

.LBB0_732:
	s_add_u32 s40, s38, 0xfff80080
	s_addc_u32 s41, s39, -1
	s_add_i32 s89, 0, 0x10000
	s_cmp_eq_u32 s88, 28
	s_cselect_b32 s43, s9, s41
	s_cselect_b32 s42, s84, s40
	v_add_u32_e32 v2, s89, v1
	s_cselect_b32 s41, s11, s87
	s_cselect_b32 s40, s85, s86
	s_add_i32 s92, 0, 0x14000
	ds_read_b128 v[144:147], v2
	ds_read_b128 v[148:151], v2 offset:1024
	ds_read_b128 v[152:155], v2 offset:2048
	ds_read_b128 v[156:159], v2 offset:3072
	v_add_u32_e32 v2, s92, v1
	ds_read_b128 v[160:163], v2
	ds_read_b128 v[164:167], v2 offset:1024
	ds_read_b128 v[168:171], v2 offset:2048
	ds_read_b128 v[172:175], v2 offset:3072
	v_lshl_add_u64 v[220:221], s[38:39], 0, v[140:141]
	s_add_i32 m0, s48, 0xc000
	ds_read_b128 v[176:179], v219
	ds_read_b128 v[180:183], v219 offset:1024
	ds_read_b128 v[184:187], v219 offset:2048
	ds_read_b128 v[188:191], v219 offset:3072
	ds_read_b128 v[192:195], v219 offset:4096
	ds_read_b128 v[196:199], v219 offset:5120
	ds_read_b128 v[200:203], v219 offset:6144
	ds_read_b128 v[204:207], v219 offset:7168
	global_load_lds_dwordx4 v[220:221], off
	v_lshl_add_u64 v[220:221], s[38:39], 0, v[142:143]
	s_add_i32 m0, s48, 0xe000
	s_nop 0
	global_load_lds_dwordx4 v[220:221], off
	s_waitcnt vmcnt(8)
	s_waitcnt lgkmcnt(0)
	s_setprio 1
	s_barrier
	v_mfma_f32_16x16x32_bf16 v[128:131], v[144:147], v[176:179], v[128:131]
	v_mfma_f32_16x16x32_bf16 v[124:127], v[152:155], v[176:179], v[124:127]
	v_mfma_f32_16x16x32_bf16 v[112:115], v[144:147], v[184:187], v[112:115]
	v_mfma_f32_16x16x32_bf16 v[108:111], v[152:155], v[184:187], v[108:111]
	v_mfma_f32_16x16x32_bf16 v[96:99], v[144:147], v[192:195], v[96:99]
	v_mfma_f32_16x16x32_bf16 v[92:95], v[152:155], v[192:195], v[92:95]
	v_mfma_f32_16x16x32_bf16 v[80:83], v[144:147], v[200:203], v[80:83]
	v_mfma_f32_16x16x32_bf16 v[76:79], v[152:155], v[200:203], v[76:79]
	v_mfma_f32_16x16x32_bf16 v[128:131], v[148:151], v[180:183], v[128:131]
	v_mfma_f32_16x16x32_bf16 v[124:127], v[156:159], v[180:183], v[124:127]
	v_mfma_f32_16x16x32_bf16 v[112:115], v[148:151], v[188:191], v[112:115]
	v_mfma_f32_16x16x32_bf16 v[108:111], v[156:159], v[188:191], v[108:111]
	v_mfma_f32_16x16x32_bf16 v[96:99], v[148:151], v[196:199], v[96:99]
	v_mfma_f32_16x16x32_bf16 v[92:95], v[156:159], v[196:199], v[92:95]
	v_mfma_f32_16x16x32_bf16 v[80:83], v[148:151], v[204:207], v[80:83]
	v_mfma_f32_16x16x32_bf16 v[76:79], v[156:159], v[204:207], v[76:79]
	s_setprio 0
	s_setprio 1
	v_mfma_f32_16x16x32_bf16 v[120:123], v[160:163], v[176:179], v[120:123]
	v_mfma_f32_16x16x32_bf16 v[116:119], v[168:171], v[176:179], v[116:119]
	v_mfma_f32_16x16x32_bf16 v[104:107], v[160:163], v[184:187], v[104:107]
	v_mfma_f32_16x16x32_bf16 v[100:103], v[168:171], v[184:187], v[100:103]
	v_mfma_f32_16x16x32_bf16 v[88:91], v[160:163], v[192:195], v[88:91]
	v_mfma_f32_16x16x32_bf16 v[84:87], v[168:171], v[192:195], v[84:87]
	v_mfma_f32_16x16x32_bf16 v[72:75], v[160:163], v[200:203], v[72:75]
	v_mfma_f32_16x16x32_bf16 v[68:71], v[168:171], v[200:203], v[68:71]
	v_mfma_f32_16x16x32_bf16 v[120:123], v[164:167], v[180:183], v[120:123]
	v_mfma_f32_16x16x32_bf16 v[116:119], v[172:175], v[180:183], v[116:119]
	v_mfma_f32_16x16x32_bf16 v[104:107], v[164:167], v[188:191], v[104:107]
	v_mfma_f32_16x16x32_bf16 v[100:103], v[172:175], v[188:191], v[100:103]
	v_mfma_f32_16x16x32_bf16 v[88:91], v[164:167], v[196:199], v[88:91]
	v_mfma_f32_16x16x32_bf16 v[84:87], v[172:175], v[196:199], v[84:87]
	v_mfma_f32_16x16x32_bf16 v[72:75], v[164:167], v[204:207], v[72:75]
	v_mfma_f32_16x16x32_bf16 v[68:71], v[172:175], v[204:207], v[68:71]
	s_setprio 0
	s_barrier
	s_add_i32 s89, s89, s45
	v_lshl_add_u64 v[220:221], s[40:41], 0, v[136:137]
	s_mov_b32 m0, s89
	ds_read_b128 v[176:179], v219 offset:16384
	ds_read_b128 v[180:183], v219 offset:17408
	ds_read_b128 v[184:187], v219 offset:18432
	ds_read_b128 v[188:191], v219 offset:19456
	ds_read_b128 v[192:195], v219 offset:20480
	ds_read_b128 v[196:199], v219 offset:21504
	ds_read_b128 v[200:203], v219 offset:22528
	ds_read_b128 v[204:207], v219 offset:23552
	global_load_lds_dwordx4 v[220:221], off
	s_add_i32 m0, s89, 0x2000
	s_add_u32 s90, s40, 0x80000
	v_lshl_add_u64 v[222:223], s[40:41], 0, v[132:133]
	s_addc_u32 s91, s41, 0
	s_add_i32 s89, s92, s45
	global_load_lds_dwordx4 v[222:223], off
	v_lshl_add_u64 v[224:225], s[90:91], 0, v[136:137]
	s_mov_b32 m0, s89
	v_lshl_add_u64 v[226:227], s[42:43], 0, v[134:135]
	global_load_lds_dwordx4 v[224:225], off
	v_lshl_add_u64 v[224:225], s[90:91], 0, v[132:133]
	s_add_i32 m0, s89, 0x2000
	s_nop 0
	global_load_lds_dwordx4 v[224:225], off
	v_lshl_add_u64 v[224:225], s[42:43], 0, v[138:139]
	s_mov_b32 m0, s48
	s_nop 0
	global_load_lds_dwordx4 v[224:225], off
	s_mov_b32 m0, s49
	s_nop 0
	global_load_lds_dwordx4 v[226:227], off
	s_waitcnt vmcnt(8)
	s_waitcnt lgkmcnt(0)
	s_setprio 1
	s_barrier
	v_mfma_f32_16x16x32_bf16 v[64:67], v[144:147], v[176:179], v[64:67]
	v_mfma_f32_16x16x32_bf16 v[60:63], v[152:155], v[176:179], v[60:63]
	v_mfma_f32_16x16x32_bf16 v[48:51], v[144:147], v[184:187], v[48:51]
	v_mfma_f32_16x16x32_bf16 v[44:47], v[152:155], v[184:187], v[44:47]
	v_mfma_f32_16x16x32_bf16 v[32:35], v[144:147], v[192:195], v[32:35]
	v_mfma_f32_16x16x32_bf16 v[28:31], v[152:155], v[192:195], v[28:31]
	v_mfma_f32_16x16x32_bf16 v[16:19], v[144:147], v[200:203], v[16:19]
	v_mfma_f32_16x16x32_bf16 v[12:15], v[152:155], v[200:203], v[12:15]
	v_mfma_f32_16x16x32_bf16 v[64:67], v[148:151], v[180:183], v[64:67]
	v_mfma_f32_16x16x32_bf16 v[60:63], v[156:159], v[180:183], v[60:63]
	v_mfma_f32_16x16x32_bf16 v[48:51], v[148:151], v[188:191], v[48:51]
	v_mfma_f32_16x16x32_bf16 v[44:47], v[156:159], v[188:191], v[44:47]
	v_mfma_f32_16x16x32_bf16 v[32:35], v[148:151], v[196:199], v[32:35]
	v_mfma_f32_16x16x32_bf16 v[28:31], v[156:159], v[196:199], v[28:31]
	v_mfma_f32_16x16x32_bf16 v[16:19], v[148:151], v[204:207], v[16:19]
	v_mfma_f32_16x16x32_bf16 v[12:15], v[156:159], v[204:207], v[12:15]
	s_setprio 0
	s_setprio 1
	v_mfma_f32_16x16x32_bf16 v[56:59], v[160:163], v[176:179], v[56:59]
	v_mfma_f32_16x16x32_bf16 v[52:55], v[168:171], v[176:179], v[52:55]
	v_mfma_f32_16x16x32_bf16 v[40:43], v[160:163], v[184:187], v[40:43]
	v_mfma_f32_16x16x32_bf16 v[36:39], v[168:171], v[184:187], v[36:39]
	v_mfma_f32_16x16x32_bf16 v[24:27], v[160:163], v[192:195], v[24:27]
	v_mfma_f32_16x16x32_bf16 v[20:23], v[168:171], v[192:195], v[20:23]
	v_mfma_f32_16x16x32_bf16 v[8:11], v[160:163], v[200:203], v[8:11]
	v_mfma_f32_16x16x32_bf16 v[4:7], v[168:171], v[200:203], v[4:7]
	v_mfma_f32_16x16x32_bf16 v[56:59], v[164:167], v[180:183], v[56:59]
	v_mfma_f32_16x16x32_bf16 v[52:55], v[172:175], v[180:183], v[52:55]
	v_mfma_f32_16x16x32_bf16 v[40:43], v[164:167], v[188:191], v[40:43]
	v_mfma_f32_16x16x32_bf16 v[36:39], v[172:175], v[188:191], v[36:39]
	v_mfma_f32_16x16x32_bf16 v[24:27], v[164:167], v[196:199], v[24:27]
	v_mfma_f32_16x16x32_bf16 v[20:23], v[172:175], v[196:199], v[20:23]
	v_mfma_f32_16x16x32_bf16 v[8:11], v[164:167], v[204:207], v[8:11]
	v_mfma_f32_16x16x32_bf16 v[4:7], v[172:175], v[204:207], v[4:7]
	s_setprio 0
	s_barrier
	s_add_i32 s89, 0, 0x18000
	v_add_u32_e32 v2, s89, v1
	s_add_i32 s90, 0, 0x1c000
	ds_read_b128 v[144:147], v2
	ds_read_b128 v[148:151], v2 offset:1024
	ds_read_b128 v[152:155], v2 offset:2048
	ds_read_b128 v[156:159], v2 offset:3072
	v_add_u32_e32 v2, s90, v1
	ds_read_b128 v[160:163], v2
	ds_read_b128 v[164:167], v2 offset:1024
	ds_read_b128 v[168:171], v2 offset:2048
	ds_read_b128 v[172:175], v2 offset:3072
	s_add_u32 s42, s42, 0x80000
	s_addc_u32 s43, s43, 0
	s_mov_b32 m0, s51
	v_lshl_add_u64 v[228:229], s[42:43], 0, v[138:139]
	ds_read_b128 v[176:179], v219 offset:32768
	ds_read_b128 v[180:183], v219 offset:33792
	ds_read_b128 v[184:187], v219 offset:34816
	ds_read_b128 v[188:191], v219 offset:35840
	ds_read_b128 v[192:195], v219 offset:36864
	ds_read_b128 v[196:199], v219 offset:37888
	ds_read_b128 v[200:203], v219 offset:38912
	ds_read_b128 v[204:207], v219 offset:39936
	global_load_lds_dwordx4 v[228:229], off
	v_lshl_add_u64 v[228:229], s[42:43], 0, v[134:135]
	s_mov_b32 m0, s60
	s_nop 0
	global_load_lds_dwordx4 v[228:229], off
	s_waitcnt vmcnt(8)
	s_waitcnt lgkmcnt(0)
	s_setprio 1
	s_barrier
	v_mfma_f32_16x16x32_bf16 v[128:131], v[144:147], v[176:179], v[128:131]
	v_mfma_f32_16x16x32_bf16 v[124:127], v[152:155], v[176:179], v[124:127]
	v_mfma_f32_16x16x32_bf16 v[112:115], v[144:147], v[184:187], v[112:115]
	v_mfma_f32_16x16x32_bf16 v[108:111], v[152:155], v[184:187], v[108:111]
	v_mfma_f32_16x16x32_bf16 v[96:99], v[144:147], v[192:195], v[96:99]
	v_mfma_f32_16x16x32_bf16 v[92:95], v[152:155], v[192:195], v[92:95]
	v_mfma_f32_16x16x32_bf16 v[80:83], v[144:147], v[200:203], v[80:83]
	v_mfma_f32_16x16x32_bf16 v[76:79], v[152:155], v[200:203], v[76:79]
	v_mfma_f32_16x16x32_bf16 v[128:131], v[148:151], v[180:183], v[128:131]
	v_mfma_f32_16x16x32_bf16 v[124:127], v[156:159], v[180:183], v[124:127]
	v_mfma_f32_16x16x32_bf16 v[112:115], v[148:151], v[188:191], v[112:115]
	v_mfma_f32_16x16x32_bf16 v[108:111], v[156:159], v[188:191], v[108:111]
	v_mfma_f32_16x16x32_bf16 v[96:99], v[148:151], v[196:199], v[96:99]
	v_mfma_f32_16x16x32_bf16 v[92:95], v[156:159], v[196:199], v[92:95]
	v_mfma_f32_16x16x32_bf16 v[80:83], v[148:151], v[204:207], v[80:83]
	v_mfma_f32_16x16x32_bf16 v[76:79], v[156:159], v[204:207], v[76:79]
	s_setprio 0
	s_setprio 1
	v_mfma_f32_16x16x32_bf16 v[120:123], v[160:163], v[176:179], v[120:123]
	v_mfma_f32_16x16x32_bf16 v[116:119], v[168:171], v[176:179], v[116:119]
	v_mfma_f32_16x16x32_bf16 v[104:107], v[160:163], v[184:187], v[104:107]
	v_mfma_f32_16x16x32_bf16 v[100:103], v[168:171], v[184:187], v[100:103]
	v_mfma_f32_16x16x32_bf16 v[88:91], v[160:163], v[192:195], v[88:91]
	v_mfma_f32_16x16x32_bf16 v[84:87], v[168:171], v[192:195], v[84:87]
	v_mfma_f32_16x16x32_bf16 v[72:75], v[160:163], v[200:203], v[72:75]
	v_mfma_f32_16x16x32_bf16 v[68:71], v[168:171], v[200:203], v[68:71]
	v_mfma_f32_16x16x32_bf16 v[120:123], v[164:167], v[180:183], v[120:123]
	v_mfma_f32_16x16x32_bf16 v[116:119], v[172:175], v[180:183], v[116:119]
	v_mfma_f32_16x16x32_bf16 v[104:107], v[164:167], v[188:191], v[104:107]
	v_mfma_f32_16x16x32_bf16 v[100:103], v[172:175], v[188:191], v[100:103]
	v_mfma_f32_16x16x32_bf16 v[88:91], v[164:167], v[196:199], v[88:91]
	v_mfma_f32_16x16x32_bf16 v[84:87], v[172:175], v[196:199], v[84:87]
	v_mfma_f32_16x16x32_bf16 v[72:75], v[164:167], v[204:207], v[72:75]
	v_mfma_f32_16x16x32_bf16 v[68:71], v[172:175], v[204:207], v[68:71]
	s_setprio 0
	s_barrier
	s_add_i32 s42, s89, s45
	v_lshl_add_u64 v[220:221], v[220:221], 0, s[16:17]
	s_mov_b32 m0, s42
	ds_read_b128 v[176:179], v219 offset:49152
	ds_read_b128 v[180:183], v219 offset:50176
	ds_read_b128 v[184:187], v219 offset:51200
	ds_read_b128 v[188:191], v219 offset:52224
	ds_read_b128 v[192:195], v219 offset:53248
	ds_read_b128 v[196:199], v219 offset:54272
	ds_read_b128 v[200:203], v219 offset:55296
	ds_read_b128 v[204:207], v219 offset:56320
	global_load_lds_dwordx4 v[220:221], off
	s_add_i32 m0, s42, 0x2000
	s_add_u32 s40, s40, 0x80080
	v_lshl_add_u64 v[220:221], v[222:223], 0, s[16:17]
	s_addc_u32 s41, s41, 0
	s_add_i32 s42, s90, s45
	global_load_lds_dwordx4 v[220:221], off
	v_lshl_add_u64 v[220:221], s[40:41], 0, v[136:137]
	s_mov_b32 m0, s42
	s_nop 0
	global_load_lds_dwordx4 v[220:221], off
	v_lshl_add_u64 v[220:221], s[40:41], 0, v[132:133]
	s_add_i32 m0, s42, 0x2000
	s_nop 0
	global_load_lds_dwordx4 v[220:221], off
	v_lshl_add_u64 v[220:221], v[224:225], 0, s[16:17]
	s_mov_b32 m0, s61
	s_nop 0
	global_load_lds_dwordx4 v[220:221], off
	v_lshl_add_u64 v[220:221], v[226:227], 0, s[16:17]
	s_mov_b32 m0, s80
	s_nop 0
	global_load_lds_dwordx4 v[220:221], off
	s_waitcnt vmcnt(8)
	s_waitcnt lgkmcnt(0)
	s_setprio 1
	s_barrier
	v_mfma_f32_16x16x32_bf16 v[64:67], v[144:147], v[176:179], v[64:67]
	v_mfma_f32_16x16x32_bf16 v[60:63], v[152:155], v[176:179], v[60:63]
	v_mfma_f32_16x16x32_bf16 v[48:51], v[144:147], v[184:187], v[48:51]
	v_mfma_f32_16x16x32_bf16 v[44:47], v[152:155], v[184:187], v[44:47]
	v_mfma_f32_16x16x32_bf16 v[32:35], v[144:147], v[192:195], v[32:35]
	v_mfma_f32_16x16x32_bf16 v[28:31], v[152:155], v[192:195], v[28:31]
	v_mfma_f32_16x16x32_bf16 v[16:19], v[144:147], v[200:203], v[16:19]
	v_mfma_f32_16x16x32_bf16 v[12:15], v[152:155], v[200:203], v[12:15]
	v_mfma_f32_16x16x32_bf16 v[64:67], v[148:151], v[180:183], v[64:67]
	v_mfma_f32_16x16x32_bf16 v[60:63], v[156:159], v[180:183], v[60:63]
	v_mfma_f32_16x16x32_bf16 v[48:51], v[148:151], v[188:191], v[48:51]
	v_mfma_f32_16x16x32_bf16 v[44:47], v[156:159], v[188:191], v[44:47]
	v_mfma_f32_16x16x32_bf16 v[32:35], v[148:151], v[196:199], v[32:35]
	v_mfma_f32_16x16x32_bf16 v[28:31], v[156:159], v[196:199], v[28:31]
	v_mfma_f32_16x16x32_bf16 v[16:19], v[148:151], v[204:207], v[16:19]
	v_mfma_f32_16x16x32_bf16 v[12:15], v[156:159], v[204:207], v[12:15]
	s_setprio 0
	s_setprio 1
	v_mfma_f32_16x16x32_bf16 v[56:59], v[160:163], v[176:179], v[56:59]
	v_mfma_f32_16x16x32_bf16 v[52:55], v[168:171], v[176:179], v[52:55]
	v_mfma_f32_16x16x32_bf16 v[40:43], v[160:163], v[184:187], v[40:43]
	v_mfma_f32_16x16x32_bf16 v[36:39], v[168:171], v[184:187], v[36:39]
	v_mfma_f32_16x16x32_bf16 v[24:27], v[160:163], v[192:195], v[24:27]
	v_mfma_f32_16x16x32_bf16 v[20:23], v[168:171], v[192:195], v[20:23]
	v_mfma_f32_16x16x32_bf16 v[8:11], v[160:163], v[200:203], v[8:11]
	v_mfma_f32_16x16x32_bf16 v[4:7], v[168:171], v[200:203], v[4:7]
	v_mfma_f32_16x16x32_bf16 v[56:59], v[164:167], v[180:183], v[56:59]
	v_mfma_f32_16x16x32_bf16 v[52:55], v[172:175], v[180:183], v[52:55]
	v_mfma_f32_16x16x32_bf16 v[40:43], v[164:167], v[188:191], v[40:43]
	v_mfma_f32_16x16x32_bf16 v[36:39], v[172:175], v[188:191], v[36:39]
	v_mfma_f32_16x16x32_bf16 v[24:27], v[164:167], v[196:199], v[24:27]
	v_mfma_f32_16x16x32_bf16 v[20:23], v[172:175], v[196:199], v[20:23]
	v_mfma_f32_16x16x32_bf16 v[8:11], v[164:167], v[204:207], v[8:11]
	v_mfma_f32_16x16x32_bf16 v[4:7], v[172:175], v[204:207], v[4:7]
	s_setprio 0
	s_barrier
	s_add_i32 s88, s88, 2
	s_add_u32 s38, s38, 0x100
	s_addc_u32 s39, s39, 0
	s_add_u32 s86, s86, 0x100
	s_addc_u32 s87, s87, 0
	s_cmp_gt_u32 s88, 29
	s_cbranch_scc0 .LBB0_732
	s_and_b64 vcc, exec, s[4:5]
	v_readlane_b32 s84, v239, 39
	s_mov_b32 s85, 0xf800000
	s_cbranch_vccz .LBB0_735
	s_barrier

.LBB0_805:
	s_add_u32 s40, s38, 0xfff80080
	s_addc_u32 s41, s39, -1
	s_add_i32 s89, 0, 0x10000
	s_cmp_eq_u32 s88, 28
	s_cselect_b32 s43, s9, s41
	s_cselect_b32 s42, s84, s40
	s_cselect_b32 s41, s11, s87
	s_cselect_b32 s40, s85, s86
	s_add_i32 s92, 0, 0x14000
	v_add_u32_e32 v158, s89, v144
	v_add_u32_e32 v174, s92, v144
	ds_read_b128 v[146:149], v158
	ds_read_b128 v[150:153], v158 offset:1024
	ds_read_b128 v[154:157], v158 offset:2048
	ds_read_b128 v[158:161], v158 offset:3072
	ds_read_b128 v[162:165], v174
	ds_read_b128 v[166:169], v174 offset:1024
	ds_read_b128 v[170:173], v174 offset:2048
	ds_read_b128 v[174:177], v174 offset:3072
	v_lshl_add_u64 v[206:207], s[38:39], 0, v[140:141]
	s_add_i32 m0, s48, 0xc000
	ds_read_b128 v[178:181], v145
	ds_read_b128 v[182:185], v145 offset:1024
	ds_read_b128 v[186:189], v145 offset:2048
	ds_read_b128 v[190:193], v145 offset:3072
	ds_read_b128 v[194:197], v145 offset:4096
	ds_read_b128 v[198:201], v145 offset:5120
	ds_read_b128 v[202:205], v145 offset:6144
	ds_read_b128 v[218:221], v145 offset:7168
	global_load_lds_dwordx4 v[206:207], off
	v_lshl_add_u64 v[206:207], s[38:39], 0, v[142:143]
	s_add_i32 m0, s48, 0xe000
	s_nop 0
	global_load_lds_dwordx4 v[206:207], off
	s_waitcnt vmcnt(8)
	s_waitcnt lgkmcnt(0)
	s_setprio 1
	s_barrier
	v_mfma_f32_16x16x32_bf16 v[128:131], v[146:149], v[178:181], v[128:131]
	v_mfma_f32_16x16x32_bf16 v[124:127], v[154:157], v[178:181], v[124:127]
	v_mfma_f32_16x16x32_bf16 v[120:123], v[146:149], v[186:189], v[120:123]
	v_mfma_f32_16x16x32_bf16 v[116:119], v[154:157], v[186:189], v[116:119]
	v_mfma_f32_16x16x32_bf16 v[104:107], v[146:149], v[194:197], v[104:107]
	v_mfma_f32_16x16x32_bf16 v[100:103], v[154:157], v[194:197], v[100:103]
	v_mfma_f32_16x16x32_bf16 v[88:91], v[146:149], v[202:205], v[88:91]
	v_mfma_f32_16x16x32_bf16 v[84:87], v[154:157], v[202:205], v[84:87]
	v_mfma_f32_16x16x32_bf16 v[128:131], v[150:153], v[182:185], v[128:131]
	v_mfma_f32_16x16x32_bf16 v[124:127], v[158:161], v[182:185], v[124:127]
	v_mfma_f32_16x16x32_bf16 v[120:123], v[150:153], v[190:193], v[120:123]
	v_mfma_f32_16x16x32_bf16 v[116:119], v[158:161], v[190:193], v[116:119]
	v_mfma_f32_16x16x32_bf16 v[104:107], v[150:153], v[198:201], v[104:107]
	v_mfma_f32_16x16x32_bf16 v[100:103], v[158:161], v[198:201], v[100:103]
	v_mfma_f32_16x16x32_bf16 v[88:91], v[150:153], v[218:221], v[88:91]
	v_mfma_f32_16x16x32_bf16 v[84:87], v[158:161], v[218:221], v[84:87]
	s_setprio 0
	s_setprio 1
	v_mfma_f32_16x16x32_bf16 v[112:115], v[162:165], v[178:181], v[112:115]
	v_mfma_f32_16x16x32_bf16 v[108:111], v[170:173], v[178:181], v[108:111]
	v_mfma_f32_16x16x32_bf16 v[96:99], v[162:165], v[186:189], v[96:99]
	v_mfma_f32_16x16x32_bf16 v[92:95], v[170:173], v[186:189], v[92:95]
	v_mfma_f32_16x16x32_bf16 v[80:83], v[162:165], v[194:197], v[80:83]
	v_mfma_f32_16x16x32_bf16 v[76:79], v[170:173], v[194:197], v[76:79]
	v_mfma_f32_16x16x32_bf16 v[72:75], v[162:165], v[202:205], v[72:75]
	v_mfma_f32_16x16x32_bf16 v[68:71], v[170:173], v[202:205], v[68:71]
	v_mfma_f32_16x16x32_bf16 v[112:115], v[166:169], v[182:185], v[112:115]
	v_mfma_f32_16x16x32_bf16 v[108:111], v[174:177], v[182:185], v[108:111]
	v_mfma_f32_16x16x32_bf16 v[96:99], v[166:169], v[190:193], v[96:99]
	v_mfma_f32_16x16x32_bf16 v[92:95], v[174:177], v[190:193], v[92:95]
	v_mfma_f32_16x16x32_bf16 v[80:83], v[166:169], v[198:201], v[80:83]
	v_mfma_f32_16x16x32_bf16 v[76:79], v[174:177], v[198:201], v[76:79]
	v_mfma_f32_16x16x32_bf16 v[72:75], v[166:169], v[218:221], v[72:75]
	v_mfma_f32_16x16x32_bf16 v[68:71], v[174:177], v[218:221], v[68:71]
	s_setprio 0
	s_barrier
	s_add_i32 s89, s89, s45
	v_lshl_add_u64 v[206:207], s[40:41], 0, v[2:3]
	s_mov_b32 m0, s89
	ds_read_b128 v[178:181], v145 offset:16384
	ds_read_b128 v[182:185], v145 offset:17408
	ds_read_b128 v[186:189], v145 offset:18432
	ds_read_b128 v[190:193], v145 offset:19456
	ds_read_b128 v[194:197], v145 offset:20480
	ds_read_b128 v[198:201], v145 offset:21504
	ds_read_b128 v[202:205], v145 offset:22528
	ds_read_b128 v[218:221], v145 offset:23552
	global_load_lds_dwordx4 v[206:207], off
	s_add_i32 m0, s89, 0x2000
	s_add_u32 s90, s40, 0x80000
	v_lshl_add_u64 v[222:223], s[40:41], 0, v[132:133]
	s_addc_u32 s91, s41, 0
	s_add_i32 s89, s92, s45
	global_load_lds_dwordx4 v[222:223], off
	v_lshl_add_u64 v[224:225], s[90:91], 0, v[2:3]
	s_mov_b32 m0, s89
	v_lshl_add_u64 v[226:227], s[42:43], 0, v[134:135]
	global_load_lds_dwordx4 v[224:225], off
	v_lshl_add_u64 v[224:225], s[90:91], 0, v[132:133]
	s_add_i32 m0, s89, 0x2000
	s_nop 0
	global_load_lds_dwordx4 v[224:225], off
	v_lshl_add_u64 v[224:225], s[42:43], 0, v[136:137]
	s_mov_b32 m0, s48
	s_nop 0
	global_load_lds_dwordx4 v[224:225], off
	s_mov_b32 m0, s49
	s_nop 0
	global_load_lds_dwordx4 v[226:227], off
	s_waitcnt vmcnt(8)
	s_waitcnt lgkmcnt(0)
	s_setprio 1
	s_barrier
	v_mfma_f32_16x16x32_bf16 v[64:67], v[146:149], v[178:181], v[64:67]
	v_mfma_f32_16x16x32_bf16 v[60:63], v[154:157], v[178:181], v[60:63]
	v_mfma_f32_16x16x32_bf16 v[56:59], v[146:149], v[186:189], v[56:59]
	v_mfma_f32_16x16x32_bf16 v[52:55], v[154:157], v[186:189], v[52:55]
	v_mfma_f32_16x16x32_bf16 v[40:43], v[146:149], v[194:197], v[40:43]
	v_mfma_f32_16x16x32_bf16 v[36:39], v[154:157], v[194:197], v[36:39]
	v_mfma_f32_16x16x32_bf16 v[24:27], v[146:149], v[202:205], v[24:27]
	v_mfma_f32_16x16x32_bf16 v[20:23], v[154:157], v[202:205], v[20:23]
	v_mfma_f32_16x16x32_bf16 v[64:67], v[150:153], v[182:185], v[64:67]
	v_mfma_f32_16x16x32_bf16 v[60:63], v[158:161], v[182:185], v[60:63]
	v_mfma_f32_16x16x32_bf16 v[56:59], v[150:153], v[190:193], v[56:59]
	v_mfma_f32_16x16x32_bf16 v[52:55], v[158:161], v[190:193], v[52:55]
	v_mfma_f32_16x16x32_bf16 v[40:43], v[150:153], v[198:201], v[40:43]
	v_mfma_f32_16x16x32_bf16 v[36:39], v[158:161], v[198:201], v[36:39]
	v_mfma_f32_16x16x32_bf16 v[24:27], v[150:153], v[218:221], v[24:27]
	v_mfma_f32_16x16x32_bf16 v[20:23], v[158:161], v[218:221], v[20:23]
	s_setprio 0
	s_setprio 1
	v_mfma_f32_16x16x32_bf16 v[48:51], v[162:165], v[178:181], v[48:51]
	v_mfma_f32_16x16x32_bf16 v[44:47], v[170:173], v[178:181], v[44:47]
	v_mfma_f32_16x16x32_bf16 v[32:35], v[162:165], v[186:189], v[32:35]
	v_mfma_f32_16x16x32_bf16 v[28:31], v[170:173], v[186:189], v[28:31]
	v_mfma_f32_16x16x32_bf16 v[16:19], v[162:165], v[194:197], v[16:19]
	v_mfma_f32_16x16x32_bf16 v[12:15], v[170:173], v[194:197], v[12:15]
	v_mfma_f32_16x16x32_bf16 v[8:11], v[162:165], v[202:205], v[8:11]
	v_mfma_f32_16x16x32_bf16 v[4:7], v[170:173], v[202:205], v[4:7]
	v_mfma_f32_16x16x32_bf16 v[48:51], v[166:169], v[182:185], v[48:51]
	v_mfma_f32_16x16x32_bf16 v[44:47], v[174:177], v[182:185], v[44:47]
	v_mfma_f32_16x16x32_bf16 v[32:35], v[166:169], v[190:193], v[32:35]
	v_mfma_f32_16x16x32_bf16 v[28:31], v[174:177], v[190:193], v[28:31]
	v_mfma_f32_16x16x32_bf16 v[16:19], v[166:169], v[198:201], v[16:19]
	v_mfma_f32_16x16x32_bf16 v[12:15], v[174:177], v[198:201], v[12:15]
	v_mfma_f32_16x16x32_bf16 v[8:11], v[166:169], v[218:221], v[8:11]
	v_mfma_f32_16x16x32_bf16 v[4:7], v[174:177], v[218:221], v[4:7]
	s_setprio 0
	s_barrier
	s_add_i32 s89, 0, 0x18000
	s_add_i32 s90, 0, 0x1c000
	v_add_u32_e32 v158, s89, v144
	v_add_u32_e32 v174, s90, v144
	ds_read_b128 v[146:149], v158
	ds_read_b128 v[150:153], v158 offset:1024
	ds_read_b128 v[154:157], v158 offset:2048
	ds_read_b128 v[158:161], v158 offset:3072
	ds_read_b128 v[162:165], v174
	ds_read_b128 v[166:169], v174 offset:1024
	ds_read_b128 v[170:173], v174 offset:2048
	ds_read_b128 v[174:177], v174 offset:3072
	s_add_u32 s42, s42, 0x80000
	s_addc_u32 s43, s43, 0
	s_mov_b32 m0, s51
	v_lshl_add_u64 v[228:229], s[42:43], 0, v[136:137]
	ds_read_b128 v[178:181], v145 offset:32768
	ds_read_b128 v[182:185], v145 offset:33792
	ds_read_b128 v[186:189], v145 offset:34816
	ds_read_b128 v[190:193], v145 offset:35840
	ds_read_b128 v[194:197], v145 offset:36864
	ds_read_b128 v[198:201], v145 offset:37888
	ds_read_b128 v[202:205], v145 offset:38912
	ds_read_b128 v[218:221], v145 offset:39936
	global_load_lds_dwordx4 v[228:229], off
	v_lshl_add_u64 v[228:229], s[42:43], 0, v[134:135]
	s_mov_b32 m0, s60
	s_nop 0
	global_load_lds_dwordx4 v[228:229], off
	s_waitcnt vmcnt(8)
	s_waitcnt lgkmcnt(0)
	s_setprio 1
	s_barrier
	v_mfma_f32_16x16x32_bf16 v[128:131], v[146:149], v[178:181], v[128:131]
	v_mfma_f32_16x16x32_bf16 v[124:127], v[154:157], v[178:181], v[124:127]
	v_mfma_f32_16x16x32_bf16 v[120:123], v[146:149], v[186:189], v[120:123]
	v_mfma_f32_16x16x32_bf16 v[116:119], v[154:157], v[186:189], v[116:119]
	v_mfma_f32_16x16x32_bf16 v[104:107], v[146:149], v[194:197], v[104:107]
	v_mfma_f32_16x16x32_bf16 v[100:103], v[154:157], v[194:197], v[100:103]
	v_mfma_f32_16x16x32_bf16 v[88:91], v[146:149], v[202:205], v[88:91]
	v_mfma_f32_16x16x32_bf16 v[84:87], v[154:157], v[202:205], v[84:87]
	v_mfma_f32_16x16x32_bf16 v[128:131], v[150:153], v[182:185], v[128:131]
	v_mfma_f32_16x16x32_bf16 v[124:127], v[158:161], v[182:185], v[124:127]
	v_mfma_f32_16x16x32_bf16 v[120:123], v[150:153], v[190:193], v[120:123]
	v_mfma_f32_16x16x32_bf16 v[116:119], v[158:161], v[190:193], v[116:119]
	v_mfma_f32_16x16x32_bf16 v[104:107], v[150:153], v[198:201], v[104:107]
	v_mfma_f32_16x16x32_bf16 v[100:103], v[158:161], v[198:201], v[100:103]
	v_mfma_f32_16x16x32_bf16 v[88:91], v[150:153], v[218:221], v[88:91]
	v_mfma_f32_16x16x32_bf16 v[84:87], v[158:161], v[218:221], v[84:87]
	s_setprio 0
	s_setprio 1
	v_mfma_f32_16x16x32_bf16 v[112:115], v[162:165], v[178:181], v[112:115]
	v_mfma_f32_16x16x32_bf16 v[108:111], v[170:173], v[178:181], v[108:111]
	v_mfma_f32_16x16x32_bf16 v[96:99], v[162:165], v[186:189], v[96:99]
	v_mfma_f32_16x16x32_bf16 v[92:95], v[170:173], v[186:189], v[92:95]
	v_mfma_f32_16x16x32_bf16 v[80:83], v[162:165], v[194:197], v[80:83]
	v_mfma_f32_16x16x32_bf16 v[76:79], v[170:173], v[194:197], v[76:79]
	v_mfma_f32_16x16x32_bf16 v[72:75], v[162:165], v[202:205], v[72:75]
	v_mfma_f32_16x16x32_bf16 v[68:71], v[170:173], v[202:205], v[68:71]
	v_mfma_f32_16x16x32_bf16 v[112:115], v[166:169], v[182:185], v[112:115]
	v_mfma_f32_16x16x32_bf16 v[108:111], v[174:177], v[182:185], v[108:111]
	v_mfma_f32_16x16x32_bf16 v[96:99], v[166:169], v[190:193], v[96:99]
	v_mfma_f32_16x16x32_bf16 v[92:95], v[174:177], v[190:193], v[92:95]
	v_mfma_f32_16x16x32_bf16 v[80:83], v[166:169], v[198:201], v[80:83]
	v_mfma_f32_16x16x32_bf16 v[76:79], v[174:177], v[198:201], v[76:79]
	v_mfma_f32_16x16x32_bf16 v[72:75], v[166:169], v[218:221], v[72:75]
	v_mfma_f32_16x16x32_bf16 v[68:71], v[174:177], v[218:221], v[68:71]
	s_setprio 0
	s_barrier
	s_add_i32 s42, s89, s45
	v_lshl_add_u64 v[206:207], v[206:207], 0, s[16:17]
	s_mov_b32 m0, s42
	ds_read_b128 v[178:181], v145 offset:49152
	ds_read_b128 v[182:185], v145 offset:50176
	ds_read_b128 v[186:189], v145 offset:51200
	ds_read_b128 v[190:193], v145 offset:52224
	ds_read_b128 v[194:197], v145 offset:53248
	ds_read_b128 v[198:201], v145 offset:54272
	ds_read_b128 v[202:205], v145 offset:55296
	ds_read_b128 v[218:221], v145 offset:56320
	global_load_lds_dwordx4 v[206:207], off
	s_add_i32 m0, s42, 0x2000
	s_add_u32 s40, s40, 0x80080
	v_lshl_add_u64 v[206:207], v[222:223], 0, s[16:17]
	s_addc_u32 s41, s41, 0
	s_add_i32 s42, s90, s45
	global_load_lds_dwordx4 v[206:207], off
	v_lshl_add_u64 v[206:207], s[40:41], 0, v[2:3]
	s_mov_b32 m0, s42
	s_nop 0
	global_load_lds_dwordx4 v[206:207], off
	v_lshl_add_u64 v[206:207], s[40:41], 0, v[132:133]
	s_add_i32 m0, s42, 0x2000
	s_nop 0
	global_load_lds_dwordx4 v[206:207], off
	v_lshl_add_u64 v[206:207], v[224:225], 0, s[16:17]
	s_mov_b32 m0, s61
	s_nop 0
	global_load_lds_dwordx4 v[206:207], off
	v_lshl_add_u64 v[206:207], v[226:227], 0, s[16:17]
	s_mov_b32 m0, s80
	s_nop 0
	global_load_lds_dwordx4 v[206:207], off
	s_waitcnt vmcnt(8)
	s_waitcnt lgkmcnt(0)
	s_setprio 1
	s_barrier
	v_mfma_f32_16x16x32_bf16 v[64:67], v[146:149], v[178:181], v[64:67]
	v_mfma_f32_16x16x32_bf16 v[60:63], v[154:157], v[178:181], v[60:63]
	v_mfma_f32_16x16x32_bf16 v[56:59], v[146:149], v[186:189], v[56:59]
	v_mfma_f32_16x16x32_bf16 v[52:55], v[154:157], v[186:189], v[52:55]
	v_mfma_f32_16x16x32_bf16 v[40:43], v[146:149], v[194:197], v[40:43]
	v_mfma_f32_16x16x32_bf16 v[36:39], v[154:157], v[194:197], v[36:39]
	v_mfma_f32_16x16x32_bf16 v[24:27], v[146:149], v[202:205], v[24:27]
	v_mfma_f32_16x16x32_bf16 v[20:23], v[154:157], v[202:205], v[20:23]
	v_mfma_f32_16x16x32_bf16 v[64:67], v[150:153], v[182:185], v[64:67]
	v_mfma_f32_16x16x32_bf16 v[60:63], v[158:161], v[182:185], v[60:63]
	v_mfma_f32_16x16x32_bf16 v[56:59], v[150:153], v[190:193], v[56:59]
	v_mfma_f32_16x16x32_bf16 v[52:55], v[158:161], v[190:193], v[52:55]
	v_mfma_f32_16x16x32_bf16 v[40:43], v[150:153], v[198:201], v[40:43]
	v_mfma_f32_16x16x32_bf16 v[36:39], v[158:161], v[198:201], v[36:39]
	v_mfma_f32_16x16x32_bf16 v[24:27], v[150:153], v[218:221], v[24:27]
	v_mfma_f32_16x16x32_bf16 v[20:23], v[158:161], v[218:221], v[20:23]
	s_setprio 0
	s_setprio 1
	v_mfma_f32_16x16x32_bf16 v[48:51], v[162:165], v[178:181], v[48:51]
	v_mfma_f32_16x16x32_bf16 v[44:47], v[170:173], v[178:181], v[44:47]
	v_mfma_f32_16x16x32_bf16 v[32:35], v[162:165], v[186:189], v[32:35]
	v_mfma_f32_16x16x32_bf16 v[28:31], v[170:173], v[186:189], v[28:31]
	v_mfma_f32_16x16x32_bf16 v[16:19], v[162:165], v[194:197], v[16:19]
	v_mfma_f32_16x16x32_bf16 v[12:15], v[170:173], v[194:197], v[12:15]
	v_mfma_f32_16x16x32_bf16 v[8:11], v[162:165], v[202:205], v[8:11]
	v_mfma_f32_16x16x32_bf16 v[4:7], v[170:173], v[202:205], v[4:7]
	v_mfma_f32_16x16x32_bf16 v[48:51], v[166:169], v[182:185], v[48:51]
	v_mfma_f32_16x16x32_bf16 v[44:47], v[174:177], v[182:185], v[44:47]
	v_mfma_f32_16x16x32_bf16 v[32:35], v[166:169], v[190:193], v[32:35]
	v_mfma_f32_16x16x32_bf16 v[28:31], v[174:177], v[190:193], v[28:31]
	v_mfma_f32_16x16x32_bf16 v[16:19], v[166:169], v[198:201], v[16:19]
	v_mfma_f32_16x16x32_bf16 v[12:15], v[174:177], v[198:201], v[12:15]
	v_mfma_f32_16x16x32_bf16 v[8:11], v[166:169], v[218:221], v[8:11]
	v_mfma_f32_16x16x32_bf16 v[4:7], v[174:177], v[218:221], v[4:7]
	s_setprio 0
	s_barrier
	s_add_i32 s88, s88, 2
	s_add_u32 s38, s38, 0x100
	s_addc_u32 s39, s39, 0
	s_add_u32 s86, s86, 0x100
	s_addc_u32 s87, s87, 0
	s_cmp_gt_u32 s88, 29
	s_cbranch_scc0 .LBB0_805
	s_and_b64 vcc, exec, s[4:5]
	v_readlane_b32 s84, v239, 39
	s_mov_b32 s85, 0xf800000
	s_cbranch_vccz .LBB0_808
	s_barrier
